# baseline (speedup 1.0000x reference)
_Z11attn_kernelPKDF16_S0_S0_PDF16_:
	s_bfe_u32 s26, s2, 0x20003
	s_load_dwordx8 s[4:11], s[0:1], 0x0
	s_lshr_b32 s1, s2, 2
	s_lshr_b32 s20, s2, 6
	v_readfirstlane_b32 s19, v0
	s_mov_b32 s21, 0
	s_lshl_b32 s27, s26, 8
	s_and_b32 s0, s2, 7
	s_and_b32 s1, s1, 8
	s_lshr_b32 s34, s19, 6
	s_lshr_b32 s55, s19, 6
	s_lshl_b64 s[12:13], s[20:21], 11
	s_xor_b32 s16, s27, 0x700
	s_or_b32 s18, s1, s0
	s_or_b32 s0, s12, s16
	s_lshl_b32 s24, s34, 5
	s_add_u32 s0, s0, s24
	s_addc_u32 s1, s13, 0
	s_lshl_b64 s[14:15], s[0:1], 10
	s_lshl_b64 s[0:1], s[0:1], 11
	s_waitcnt lgkmcnt(0)
	s_add_u32 s0, s4, s0
	s_addc_u32 s1, s5, s1
	s_lshl_b32 s33, s18, 6
	s_lshl_b32 s2, s18, 7
	s_add_u32 s2, s0, s2
	s_addc_u32 s3, s1, 0
	s_lshl_b32 s0, s20, 4
	s_or_b32 s20, s18, s0
	s_and_b32 s17, s19, 0x3fffffc0
	s_lshl_b64 s[0:1], s[20:21], 18
	s_add_u32 s28, s6, s0
	s_addc_u32 s29, s7, s1
	s_lshl_b32 s18, s34, 10
	s_add_u32 s6, s28, s18
	s_addc_u32 s7, s29, 0
	s_add_u32 s30, s8, s0
	s_addc_u32 s31, s9, s1
	s_lshl_b32 s0, s19, 4
	v_and_b32_e32 v207, 63, v0
	s_and_b32 s0, s0, 0xfffff000
	v_mov_b32_e32 v3, 0
	v_lshlrev_b32_e32 v2, 4, v207
	s_add_u32 s0, s30, s0
	v_lshl_add_u64 v[212:213], s[6:7], 0, v[2:3]
	s_addc_u32 s1, s31, 0
	s_lshr_b32 s6, s19, 2
	v_bfe_u32 v1, v0, 2, 4
	v_and_or_b32 v2, s6, 48, v1
	v_lshlrev_b32_e32 v2, 6, v2
	v_lshlrev_b32_e32 v209, 3, v0
	s_cmp_lg_u32 0, -1
	v_lshl_add_u64 v[4:5], s[0:1], 0, v[2:3]
	v_and_b32_e32 v208, 24, v209
	s_cselect_b32 s0, 0, 0
	v_and_b32_e32 v222, 31, v0
	v_lshlrev_b32_e32 v2, 1, v208
	s_add_i32 s35, s18, s0
	s_mov_b32 s0, m0
	s_mov_b32 m0, s35
	s_nop 0
	global_load_lds_dwordx4 v[212:213], off
	s_mov_b32 m0, s0
	v_bfe_u32 v6, v0, 5, 1
	v_lshlrev_b32_e32 v7, 10, v222
	v_lshl_or_b32 v6, v6, 3, v7
	v_lshlrev_b32_e32 v6, 1, v6
	global_load_dwordx4 v[158:161], v6, s[2:3]
	global_load_dwordx4 v[154:157], v6, s[2:3] offset:32
	global_load_dwordx4 v[150:153], v6, s[2:3] offset:64
	global_load_dwordx4 v[146:149], v6, s[2:3] offset:96
	v_bfe_u32 v211, v0, 5, 1
	v_lshl_add_u64 v[194:195], v[4:5], 0, v[2:3]
	s_add_i32 s39, s35, 0x6000
	s_mov_b32 s0, m0
	s_mov_b32 m0, s39
	s_nop 0
	global_load_lds_dwordx4 v[194:195], off
	s_mov_b32 m0, s0
	v_lshlrev_b32_e32 v2, 10, v222
	s_mov_b64 s[0:1], 0x2000
	v_lshl_or_b32 v210, v211, 3, v2
	v_lshl_add_u64 v[214:215], v[212:213], 0, s[0:1]
	s_add_i32 s36, s35, 0x2000
	s_mov_b32 s6, m0
	s_mov_b32 m0, s36
	s_nop 0
	global_load_lds_dwordx4 v[214:215], off
	s_mov_b32 m0, s6
	v_lshlrev_b32_e32 v2, 1, v210
	v_lshlrev_b32_e32 v4, 10, v211
	v_lshlrev_b32_e32 v5, 4, v222
	v_add3_u32 v224, 0, v4, v5
	v_mov_b32_e32 v4, v3
	v_mov_b32_e32 v5, v3
	v_mov_b32_e32 v6, v3
	v_mov_b32_e32 v7, v3
	v_mov_b32_e32 v8, v3
	v_mov_b32_e32 v9, v3
	v_mov_b32_e32 v10, v3
	v_mov_b32_e32 v11, v3
	v_mov_b32_e32 v12, v3
	v_mov_b32_e32 v13, v3
	v_mov_b32_e32 v14, v3
	v_mov_b32_e32 v15, v3
	v_mov_b32_e32 v16, v3
	v_mov_b32_e32 v17, v3
	v_mov_b32_e32 v18, v3
	v_mov_b32_e32 v19, v3
	s_mov_b64 s[2:3], 0x4000
	s_add_i32 s37, s35, 0x4000
	v_lshl_add_u64 v[216:217], v[212:213], 0, s[2:3]
	s_mov_b32 s6, m0
	s_mov_b32 m0, s37
	s_nop 0
	global_load_lds_dwordx4 v[216:217], off
	s_mov_b32 m0, s6
	s_waitcnt vmcnt(3) lgkmcnt(0)
	s_barrier
	ds_read_b128 v[36:39], v224
	ds_read_b128 v[40:43], v224 offset:512
	s_mov_b64 s[6:7], 0x6000
	s_mov_b32 s41, 3
	s_movk_i32 s46, 0x2000
	s_movk_i32 s25, 0x4000
	s_sub_i32 s43, 0xbf, s16
	s_mov_b32 s45, 0x41000000
	s_mov_b64 s[18:19], 0xa000
	v_lshlrev_b32_e32 v226, 4, v211
	v_mov_b32_e32 v233, v3
	v_lshlrev_b32_e32 v206, 3, v207
	s_waitcnt vmcnt(3) lgkmcnt(1)
	v_mfma_f32_32x32x16_f16 v[20:35], v[36:39], v[158:161], v[4:19]
	s_waitcnt lgkmcnt(0)
	v_mfma_f32_32x32x16_f16 v[4:19], v[40:43], v[158:161], v[4:19]
	ds_read_b128 v[36:39], v224 offset:2048
	ds_read_b128 v[40:43], v224 offset:2560
	s_waitcnt vmcnt(3) lgkmcnt(1)
	v_mfma_f32_32x32x16_f16 v[20:35], v[36:39], v[154:157], v[20:35]
	s_waitcnt lgkmcnt(0)
	v_mfma_f32_32x32x16_f16 v[4:19], v[40:43], v[154:157], v[4:19]
	ds_read_b128 v[36:39], v224 offset:4096
	ds_read_b128 v[40:43], v224 offset:4608
	s_waitcnt vmcnt(3) lgkmcnt(1)
	v_mfma_f32_32x32x16_f16 v[20:35], v[36:39], v[150:153], v[20:35]
	s_waitcnt lgkmcnt(0)
	v_mfma_f32_32x32x16_f16 v[4:19], v[40:43], v[150:153], v[4:19]
	ds_read_b128 v[36:39], v224 offset:6144
	ds_read_b128 v[40:43], v224 offset:6656
	s_waitcnt vmcnt(3) lgkmcnt(1)
	v_mfma_f32_32x32x16_f16 v[20:35], v[36:39], v[146:149], v[20:35]
	s_waitcnt lgkmcnt(0)
	v_mfma_f32_32x32x16_f16 v[4:19], v[40:43], v[146:149], v[4:19]
	s_nop 15
	s_nop 7
	s_nop 0
	v_max3_f32 v2, v20, v21, v4
	v_max3_f32 v36, v22, v23, v5
	s_nop 0
	v_max3_f32 v2, v2, v6, v7
	v_max3_f32 v36, v36, v26, v27
	s_nop 0
	v_max3_f32 v2, v2, v24, v25
	v_max3_f32 v36, v36, v10, v11
	s_nop 0
	v_max3_f32 v2, v2, v8, v9
	v_max3_f32 v36, v36, v30, v31
	s_nop 0
	v_max3_f32 v2, v2, v28, v29
	v_max3_f32 v36, v36, v14, v15
	s_nop 0
	v_max3_f32 v2, v2, v12, v13
	v_max3_f32 v36, v36, v34, v35
	s_nop 0
	v_max3_f32 v2, v2, v32, v33
	v_max3_f32 v36, v36, v18, v19
	s_nop 0
	v_max3_f32 v2, v2, v16, v17
	s_nop 0
	v_max_f32_e32 v2, v2, v36
	s_nop 0
	v_mov_b32_e32 v36, v2
	s_nop 1
	v_permlane32_swap_b32_e32 v2, v36
	v_max_f32_e32 v2, v2, v36
	s_nop 0
	v_sub_f32_e32 v50, v34, v2
	v_add_f32_e32 v231, v3, v2
	v_sub_f32_e32 v51, v35, v2
	v_sub_f32_e32 v52, v4, v2
	v_sub_f32_e32 v53, v5, v2
	v_lshl_add_u64 v[4:5], v[212:213], 0, s[6:7]
	v_xor_b32_e32 v34, 0x80000000, v231
	v_mov_b32_e32 v35, v34
	v_mov_b32_e32 v36, v34
	v_mov_b32_e32 v37, v34
	v_mov_b32_e32 v38, v34
	v_mov_b32_e32 v39, v34
	v_mov_b32_e32 v40, v34
	v_mov_b32_e32 v41, v34
	v_mov_b32_e32 v42, v34
	v_mov_b32_e32 v43, v34
	v_mov_b32_e32 v44, v34
	v_mov_b32_e32 v45, v34
	v_mov_b32_e32 v46, v34
	v_mov_b32_e32 v47, v34
	v_mov_b32_e32 v48, v34
	v_mov_b32_e32 v49, v34
	s_waitcnt vmcnt(0) lgkmcnt(0)
	s_barrier
	s_mov_b32 s8, m0
	s_mov_b32 m0, s35
	s_nop 0
	global_load_lds_dwordx4 v[4:5], off
	s_mov_b32 m0, s8
	s_add_i32 s8, s35, 0x8000
	v_lshl_add_u64 v[4:5], v[194:195], 0, s[0:1]
	s_mov_b32 s0, m0
	s_mov_b32 m0, s8
	s_nop 0
	global_load_lds_dwordx4 v[4:5], off
	s_mov_b32 m0, s0
	ds_read_b128 v[190:193], v224 offset:8192
	ds_read_b128 v[186:189], v224 offset:8704
	ds_read_b128 v[182:185], v224 offset:10240
	ds_read_b128 v[178:181], v224 offset:10752
	ds_read_b128 v[174:177], v224 offset:12288
	ds_read_b128 v[170:173], v224 offset:12800
	ds_read_b128 v[166:169], v224 offset:14336
	ds_read_b128 v[162:165], v224 offset:14848
	v_sub_f32_e32 v20, v20, v2
	v_sub_f32_e32 v21, v21, v2
	v_sub_f32_e32 v22, v22, v2
	v_sub_f32_e32 v23, v23, v2
	v_sub_f32_e32 v24, v24, v2
	v_sub_f32_e32 v25, v25, v2
	v_sub_f32_e32 v26, v26, v2
	v_sub_f32_e32 v27, v27, v2
	v_sub_f32_e32 v28, v28, v2
	v_sub_f32_e32 v29, v29, v2
	v_sub_f32_e32 v30, v30, v2
	v_sub_f32_e32 v31, v31, v2
	v_sub_f32_e32 v32, v32, v2
	v_sub_f32_e32 v33, v33, v2
	v_sub_f32_e32 v6, v6, v2
	v_sub_f32_e32 v7, v7, v2
	v_sub_f32_e32 v8, v8, v2
	v_sub_f32_e32 v9, v9, v2
	v_sub_f32_e32 v10, v10, v2
	v_sub_f32_e32 v11, v11, v2
	v_sub_f32_e32 v12, v12, v2
	v_sub_f32_e32 v13, v13, v2
	v_sub_f32_e32 v14, v14, v2
	v_sub_f32_e32 v15, v15, v2
	v_sub_f32_e32 v16, v16, v2
	v_sub_f32_e32 v17, v17, v2
	v_sub_f32_e32 v18, v18, v2
	v_sub_f32_e32 v19, v19, v2
	v_lshlrev_b32_e32 v2, 1, v0
	v_and_b32_e32 v228, 32, v2
	v_lshlrev_b32_e32 v2, 4, v0
	v_exp_f32_e32 v81, v51
	v_exp_f32_e32 v66, v20
	v_exp_f32_e32 v67, v21
	v_exp_f32_e32 v68, v22
	v_exp_f32_e32 v69, v23
	v_exp_f32_e32 v70, v24
	v_exp_f32_e32 v71, v25
	v_exp_f32_e32 v72, v26
	v_exp_f32_e32 v73, v27
	v_exp_f32_e32 v74, v28
	v_exp_f32_e32 v75, v29
	v_exp_f32_e32 v76, v30
	v_exp_f32_e32 v77, v31
	v_exp_f32_e32 v78, v32
	v_exp_f32_e32 v79, v33
	v_exp_f32_e32 v80, v50
	v_exp_f32_e32 v65, v19
	v_exp_f32_e32 v50, v52
	v_exp_f32_e32 v51, v53
	v_exp_f32_e32 v52, v6
	v_exp_f32_e32 v53, v7
	v_exp_f32_e32 v54, v8
	v_exp_f32_e32 v55, v9
	v_exp_f32_e32 v56, v10
	v_exp_f32_e32 v57, v11
	v_exp_f32_e32 v58, v12
	v_exp_f32_e32 v59, v13
	v_exp_f32_e32 v60, v14
	v_exp_f32_e32 v61, v15
	v_exp_f32_e32 v62, v16
	v_exp_f32_e32 v63, v17
	v_exp_f32_e32 v64, v18
	v_and_b32_e32 v2, 0xc0, v2
	s_add_i32 s0, s16, 0x100
	v_lshl_or_b32 v230, v211, 8, v2
	v_add_u32_e32 v2, 0, v228
	v_mov_b32_e32 v16, v3
	v_mov_b32_e32 v17, v3
	s_lshr_b32 s42, s0, 6
	s_lshl_b32 s0, s17, 2
	s_waitcnt vmcnt(2) lgkmcnt(0)
	s_barrier
	v_add3_u32 v225, v2, v208, v230
	v_mov_b32_e32 v2, v3
	v_mov_b32_e32 v4, v3
	v_mov_b32_e32 v5, v3
	v_mov_b32_e32 v6, v3
	v_mov_b32_e32 v7, v3
	v_mov_b32_e32 v8, v3
	v_mov_b32_e32 v9, v3
	v_mov_b32_e32 v10, v3
	v_mov_b32_e32 v11, v3
	v_mov_b32_e32 v12, v3
	v_mov_b32_e32 v13, v3
	v_mov_b32_e32 v14, v3
	v_mov_b32_e32 v15, v3
	s_add_i32 s38, s0, 0
	v_mov_b64_e32 v[32:33], v[16:17]
	v_cmp_gt_u32_e64 s[0:1], 32, v207
	s_mov_b64 s[8:9], 0
	s_mov_b64 s[16:17], 0x8000
	v_lshl_add_u32 v223, v222, 2, s38
	v_mov_b64_e32 v[30:31], v[14:15]
	v_mov_b64_e32 v[28:29], v[12:13]
	v_mov_b64_e32 v[26:27], v[10:11]
	v_mov_b64_e32 v[24:25], v[8:9]
	v_mov_b64_e32 v[22:23], v[6:7]
	v_mov_b64_e32 v[20:21], v[4:5]
	v_mov_b64_e32 v[18:19], v[2:3]
